# Hyena SEQ unit main loop: the next batch's z fragments are loaded at the top of the iteration (fresh registers) instead of late in it, mid-loop wait counted
# speedup vs baseline: 1.0060x; 1.0039x over previous
; #define LAS __attribute__((address_space(3)))
; template <int L>
; __device__ __forceinline__ void hyena_unit(CArgs& a, int l, int c, LAS unsigned char* lds) {
;     ...
;         for (int ib = 0; ib < 8; ++ib) {
;             const bf16* zq = zp + 256 * (ib < 7 ? ib + 1 : 7);
; #pragma unroll
;             for (int ii = 0; ii < 8; ++ii) zn[ii] = *(const bf16x8*)(zq + 32 * ii);
; #pragma unroll
;             for (int ii = 0; ii < 8; ++ii) {
;                 A[(16 - 2 * ii) & 15] = *(const LAS bf16x8*)(ap + 64 * ii);
;                 A[(17 - 2 * ii) & 15] = *(const LAS bf16x8*)(ap + 64 * ii - 32);
; #pragma unroll
;                 for (int jj = 0; jj < 16; ++jj) { const int j = (jj + 2) & 15; acc[j] = __builtin_amdgcn_mfma_f32_16x16x32_bf16(A[(j + 16 - 2 * ii) & 15], zc[ii], acc[j], 0, 0, 0); }
;             }
;             ap += 512;
; #pragma unroll
;             for (int ii = 0; ii < 8; ++ii) zc[ii] = zn[ii];
;         }
.LBB0_2257:
	s_waitcnt vmcnt(1) lgkmcnt(1)
	s_nop 0
	v_mfma_f32_16x16x32_bf16 v[44:47], v[56:59], v[30:33], v[44:47]
	s_cmpk_lg_i32 s14, 0x800
	s_cselect_b32 s78, s14, 0x700
	v_lshl_add_u64 v[214:215], s[78:79], 1, v[158:159]
	global_load_dwordx4 v[210:213], v[214:215], off
	global_load_dwordx4 v[170:173], v[214:215], off offset:64
	global_load_dwordx4 v[174:177], v[214:215], off offset:128
	global_load_dwordx4 v[178:181], v[214:215], off offset:192
	global_load_dwordx4 v[182:185], v[214:215], off offset:256
	global_load_dwordx4 v[186:189], v[214:215], off offset:320
	global_load_dwordx4 v[202:205], v[214:215], off offset:384
	global_load_dwordx4 v[206:209], v[214:215], off offset:448
	s_addk_i32 s14, 0x100
	v_mfma_f32_16x16x32_bf16 v[36:39], v[80:83], v[30:33], v[36:39]
	s_cmpk_lg_i32 s14, 0x900
	v_mfma_f32_16x16x32_bf16 v[44:47], v[80:83], v[26:29], v[44:47]
	v_mfma_f32_16x16x32_bf16 v[136:139], v[88:91], v[30:33], v[136:139]
	v_mfma_f32_16x16x32_bf16 v[132:135], v[84:87], v[30:33], v[132:135]
	v_mfma_f32_16x16x32_bf16 v[128:131], v[104:107], v[30:33], v[128:131]
	v_mfma_f32_16x16x32_bf16 v[124:127], v[96:99], v[30:33], v[124:127]
	v_mfma_f32_16x16x32_bf16 v[48:51], v[112:115], v[30:33], v[48:51]
	v_mfma_f32_16x16x32_bf16 v[36:39], v[112:115], v[26:29], v[36:39]
	v_mfma_f32_16x16x32_bf16 v[44:47], v[112:115], v[22:25], v[44:47]
	v_subrev_u32_e32 v112, 32, v161
	s_waitcnt lgkmcnt(0)
	v_mfma_f32_16x16x32_bf16 v[52:55], v[60:63], v[30:33], v[52:55]
	v_mfma_f32_16x16x32_bf16 v[56:59], v[72:75], v[26:29], v[136:139]
	v_mfma_f32_16x16x32_bf16 v[60:63], v[68:71], v[26:29], v[132:135]
	s_nop 1
	ds_read_b128 v[136:139], v112
	ds_read_b128 v[132:135], v161
	v_mfma_f32_16x16x32_bf16 v[128:131], v[88:91], v[26:29], v[128:131]
	v_mfma_f32_16x16x32_bf16 v[124:127], v[84:87], v[26:29], v[124:127]
	v_mfma_f32_16x16x32_bf16 v[140:143], v[68:71], v[30:33], v[140:143]
	v_mfma_f32_16x16x32_bf16 v[40:43], v[76:79], v[30:33], v[40:43]
	v_mfma_f32_16x16x32_bf16 v[52:55], v[76:79], v[26:29], v[52:55]
	v_mfma_f32_16x16x32_bf16 v[76:79], v[72:75], v[22:25], v[128:131]
	v_mfma_f32_16x16x32_bf16 v[80:83], v[68:71], v[22:25], v[124:127]
	v_mfma_f32_16x16x32_bf16 v[144:147], v[72:75], v[30:33], v[144:147]
	s_waitcnt lgkmcnt(0)
	v_mfma_f32_16x16x32_bf16 v[124:127], v[132:135], v[22:25], v[56:59]
	v_mfma_f32_16x16x32_bf16 v[128:131], v[136:139], v[26:29], v[140:143]
	v_mfma_f32_16x16x32_bf16 v[140:143], v[136:139], v[22:25], v[60:63]
	s_nop 2
	ds_read_b128 v[60:63], v161 offset:64
	ds_read_b128 v[56:59], v161 offset:32
	v_mfma_f32_16x16x32_bf16 v[120:123], v[100:103], v[30:33], v[120:123]
	v_mfma_f32_16x16x32_bf16 v[92:95], v[108:111], v[30:33], v[92:95]
	v_mfma_f32_16x16x32_bf16 v[64:67], v[116:119], v[30:33], v[64:67]
	v_mfma_f32_16x16x32_bf16 v[40:43], v[116:119], v[26:29], v[40:43]
	v_mfma_f32_16x16x32_bf16 v[52:55], v[116:119], v[22:25], v[52:55]
	v_mfma_f32_16x16x32_bf16 v[112:115], v[132:135], v[30:33], v[148:151]
	v_mfma_f32_16x16x32_bf16 v[30:33], v[136:139], v[30:33], v[152:155]
	v_mfma_f32_16x16x32_bf16 v[76:79], v[132:135], v[18:21], v[76:79]
	v_mfma_f32_16x16x32_bf16 v[80:83], v[136:139], v[18:21], v[80:83]
	v_mfma_f32_16x16x32_bf16 v[116:119], v[132:135], v[26:29], v[144:147]
	v_mfma_f32_16x16x32_bf16 v[120:123], v[104:107], v[26:29], v[120:123]
	v_mfma_f32_16x16x32_bf16 v[92:95], v[96:99], v[26:29], v[92:95]
	v_mfma_f32_16x16x32_bf16 v[64:67], v[100:103], v[26:29], v[64:67]
	v_mfma_f32_16x16x32_bf16 v[48:51], v[108:111], v[26:29], v[48:51]
	v_mfma_f32_16x16x32_bf16 v[40:43], v[100:103], v[22:25], v[40:43]
	v_mfma_f32_16x16x32_bf16 v[52:55], v[100:103], v[18:21], v[52:55]
	s_waitcnt lgkmcnt(1)
	v_mfma_f32_16x16x32_bf16 v[100:103], v[60:63], v[26:29], v[112:115]
	v_mfma_f32_16x16x32_bf16 v[112:115], v[60:63], v[18:21], v[124:127]
	s_waitcnt lgkmcnt(0)
	v_mfma_f32_16x16x32_bf16 v[26:29], v[56:59], v[26:29], v[30:33]
	v_mfma_f32_16x16x32_bf16 v[30:33], v[56:59], v[22:25], v[128:131]
	v_mfma_f32_16x16x32_bf16 v[124:127], v[60:63], v[14:17], v[76:79]
	v_mfma_f32_16x16x32_bf16 v[128:131], v[56:59], v[14:17], v[80:83]
	s_nop 1
	ds_read_b128 v[76:79], v161 offset:128
	ds_read_b128 v[80:83], v161 offset:96
	v_mfma_f32_16x16x32_bf16 v[36:39], v[108:111], v[22:25], v[36:39]
	v_mfma_f32_16x16x32_bf16 v[44:47], v[108:111], v[18:21], v[44:47]
	v_mfma_f32_16x16x32_bf16 v[108:111], v[60:63], v[22:25], v[116:119]
	v_mfma_f32_16x16x32_bf16 v[116:119], v[56:59], v[18:21], v[140:143]
	v_mfma_f32_16x16x32_bf16 v[120:123], v[88:91], v[22:25], v[120:123]
	v_mfma_f32_16x16x32_bf16 v[92:95], v[84:87], v[22:25], v[92:95]
	v_mfma_f32_16x16x32_bf16 v[64:67], v[104:107], v[22:25], v[64:67]
	v_mfma_f32_16x16x32_bf16 v[48:51], v[96:99], v[22:25], v[48:51]
	v_mfma_f32_16x16x32_bf16 v[40:43], v[104:107], v[18:21], v[40:43]
	v_mfma_f32_16x16x32_bf16 v[36:39], v[96:99], v[18:21], v[36:39]
	v_mfma_f32_16x16x32_bf16 v[52:55], v[104:107], v[14:17], v[52:55]
	v_mfma_f32_16x16x32_bf16 v[44:47], v[96:99], v[14:17], v[44:47]
	s_waitcnt lgkmcnt(1)
	v_mfma_f32_16x16x32_bf16 v[96:99], v[76:79], v[22:25], v[100:103]
	v_mfma_f32_16x16x32_bf16 v[104:107], v[76:79], v[14:17], v[112:115]
	s_waitcnt lgkmcnt(0)
; #define LAS __attribute__((address_space(3)))
; template <int L>
; __device__ __forceinline__ void hyena_unit(CArgs& a, int l, int c, LAS unsigned char* lds) {
;     ...
;         for (int ib = 0; ib < 8; ++ib) {
;             const bf16* zq = zp + 256 * (ib < 7 ? ib + 1 : 7);
; #pragma unroll
;             for (int ii = 0; ii < 8; ++ii) zn[ii] = *(const bf16x8*)(zq + 32 * ii);
; #pragma unroll
;             for (int ii = 0; ii < 8; ++ii) {
;                 A[(16 - 2 * ii) & 15] = *(const LAS bf16x8*)(ap + 64 * ii);
;                 A[(17 - 2 * ii) & 15] = *(const LAS bf16x8*)(ap + 64 * ii - 32);
; #pragma unroll
;                 for (int jj = 0; jj < 16; ++jj) { const int j = (jj + 2) & 15; acc[j] = __builtin_amdgcn_mfma_f32_16x16x32_bf16(A[(j + 16 - 2 * ii) & 15], zc[ii], acc[j], 0, 0, 0); }
;             }
;             ap += 512;
; #pragma unroll
;             for (int ii = 0; ii < 8; ++ii) zc[ii] = zn[ii];
;         }
	v_mfma_f32_16x16x32_bf16 v[22:25], v[80:83], v[22:25], v[26:29]
	v_mfma_f32_16x16x32_bf16 v[26:29], v[80:83], v[18:21], v[30:33]
	v_mfma_f32_16x16x32_bf16 v[30:33], v[80:83], v[14:17], v[116:119]
	s_nop 2
	ds_read_b128 v[116:119], v161 offset:192
	ds_read_b128 v[112:115], v161 offset:160
	v_mfma_f32_16x16x32_bf16 v[100:103], v[76:79], v[18:21], v[108:111]
	v_mfma_f32_16x16x32_bf16 v[108:111], v[76:79], v[10:13], v[124:127]
	v_mfma_f32_16x16x32_bf16 v[124:127], v[80:83], v[10:13], v[128:131]
	v_mfma_f32_16x16x32_bf16 v[120:123], v[72:75], v[18:21], v[120:123]
	v_mfma_f32_16x16x32_bf16 v[92:95], v[68:71], v[18:21], v[92:95]
	v_mfma_f32_16x16x32_bf16 v[64:67], v[88:91], v[18:21], v[64:67]
	v_mfma_f32_16x16x32_bf16 v[48:51], v[84:87], v[18:21], v[48:51]
	v_mfma_f32_16x16x32_bf16 v[40:43], v[88:91], v[14:17], v[40:43]
	v_mfma_f32_16x16x32_bf16 v[36:39], v[84:87], v[14:17], v[36:39]
	v_mfma_f32_16x16x32_bf16 v[52:55], v[88:91], v[10:13], v[52:55]
	v_mfma_f32_16x16x32_bf16 v[44:47], v[84:87], v[10:13], v[44:47]
	s_waitcnt lgkmcnt(1)
	v_mfma_f32_16x16x32_bf16 v[84:87], v[116:119], v[18:21], v[96:99]
	v_mfma_f32_16x16x32_bf16 v[88:91], v[116:119], v[14:17], v[100:103]
	s_waitcnt lgkmcnt(0)
	v_mfma_f32_16x16x32_bf16 v[18:21], v[112:115], v[18:21], v[22:25]
	v_mfma_f32_16x16x32_bf16 v[22:25], v[112:115], v[14:17], v[26:29]
	v_mfma_f32_16x16x32_bf16 v[26:29], v[112:115], v[10:13], v[30:33]
	v_mfma_f32_16x16x32_bf16 v[30:33], v[116:119], v[6:9], v[108:111]
	ds_read_b128 v[100:103], v161 offset:256
	s_nop 1
	ds_read_b128 v[108:111], v161 offset:224
	v_mfma_f32_16x16x32_bf16 v[96:99], v[116:119], v[10:13], v[104:107]
	v_mfma_f32_16x16x32_bf16 v[104:107], v[112:115], v[6:9], v[124:127]
	v_mfma_f32_16x16x32_bf16 v[48:51], v[68:71], v[14:17], v[48:51]
	v_mfma_f32_16x16x32_bf16 v[36:39], v[68:71], v[10:13], v[36:39]
	v_mfma_f32_16x16x32_bf16 v[44:47], v[68:71], v[6:9], v[44:47]
	s_waitcnt lgkmcnt(1)
	v_mfma_f32_16x16x32_bf16 v[68:71], v[100:103], v[14:17], v[84:87]
	v_mfma_f32_16x16x32_bf16 v[84:87], v[100:103], v[6:9], v[96:99]
	s_waitcnt vmcnt(8) lgkmcnt(0)
	v_mfma_f32_16x16x32_bf16 v[124:127], v[108:111], v[2:5], v[104:107]
	s_nop 2
	ds_read_b128 v[104:107], v161 offset:320
	ds_read_b128 v[96:99], v161 offset:288
	v_mfma_f32_16x16x32_bf16 v[120:123], v[132:135], v[14:17], v[120:123]
	v_mfma_f32_16x16x32_bf16 v[92:95], v[136:139], v[14:17], v[92:95]
	v_mfma_f32_16x16x32_bf16 v[64:67], v[72:75], v[14:17], v[64:67]
	v_mfma_f32_16x16x32_bf16 v[14:17], v[108:111], v[14:17], v[18:21]
	v_mfma_f32_16x16x32_bf16 v[18:21], v[108:111], v[10:13], v[22:25]
	v_mfma_f32_16x16x32_bf16 v[22:25], v[108:111], v[6:9], v[26:29]
	s_waitcnt lgkmcnt(1)
	v_mfma_f32_16x16x32_bf16 v[26:29], v[104:107], v[10:13], v[68:71]
	s_nop 2
	v_mfma_f32_16x16x32_bf16 v[120:123], v[60:63], v[10:13], v[120:123]
	v_mfma_f32_16x16x32_bf16 v[92:95], v[56:59], v[10:13], v[92:95]
	v_mfma_f32_16x16x32_bf16 v[64:67], v[132:135], v[10:13], v[64:67]
	v_mfma_f32_16x16x32_bf16 v[48:51], v[136:139], v[10:13], v[48:51]
	v_mfma_f32_16x16x32_bf16 v[40:43], v[72:75], v[10:13], v[40:43]
	v_mfma_f32_16x16x32_bf16 v[52:55], v[72:75], v[6:9], v[52:55]
	v_mfma_f32_16x16x32_bf16 v[72:75], v[100:103], v[10:13], v[88:91]
	s_waitcnt lgkmcnt(0)
	v_mfma_f32_16x16x32_bf16 v[10:13], v[96:99], v[10:13], v[14:17]
	s_nop 2
	v_mfma_f32_16x16x32_bf16 v[36:39], v[136:139], v[6:9], v[36:39]
	v_mfma_f32_16x16x32_bf16 v[44:47], v[136:139], v[2:5], v[44:47]
	v_mfma_f32_16x16x32_bf16 v[136:139], v[104:107], v[2:5], v[84:87]
	ds_read_b128 v[88:91], v161 offset:384
	s_nop 1
	ds_read_b128 v[84:87], v161 offset:352
	v_mfma_f32_16x16x32_bf16 v[128:131], v[100:103], v[2:5], v[30:33]
	ds_read_b128 v[68:71], v161 offset:416
	v_mfma_f32_16x16x32_bf16 v[30:33], v[104:107], v[6:9], v[72:75]
	s_nop 2
	ds_read_b128 v[72:75], v161 offset:448
	v_mfma_f32_16x16x32_bf16 v[120:123], v[76:79], v[6:9], v[120:123]
	v_add_u32_e32 v161, 0x200, v161
	v_mfma_f32_16x16x32_bf16 v[92:95], v[80:83], v[6:9], v[92:95]
	v_mfma_f32_16x16x32_bf16 v[64:67], v[60:63], v[6:9], v[64:67]
	v_mfma_f32_16x16x32_bf16 v[48:51], v[56:59], v[6:9], v[48:51]
	v_mfma_f32_16x16x32_bf16 v[40:43], v[132:135], v[6:9], v[40:43]
	v_mfma_f32_16x16x32_bf16 v[52:55], v[132:135], v[2:5], v[52:55]
	v_mfma_f32_16x16x32_bf16 v[18:21], v[96:99], v[6:9], v[18:21]
	v_mfma_f32_16x16x32_bf16 v[132:135], v[96:99], v[2:5], v[22:25]
	s_waitcnt lgkmcnt(3)
	v_mfma_f32_16x16x32_bf16 v[22:25], v[88:91], v[6:9], v[26:29]
	s_waitcnt lgkmcnt(2)
	v_mfma_f32_16x16x32_bf16 v[6:9], v[84:87], v[6:9], v[10:13]
	s_waitcnt vmcnt(6)
	v_mov_b64_e32 v[26:27], v[170:171]
	v_mfma_f32_16x16x32_bf16 v[120:123], v[116:119], v[2:5], v[120:123]
	v_mov_b64_e32 v[28:29], v[172:173]
	s_waitcnt vmcnt(2)
	v_mov_b64_e32 v[10:11], v[186:187]
	v_mfma_f32_16x16x32_bf16 v[92:95], v[112:115], v[2:5], v[92:95]
	v_mov_b64_e32 v[12:13], v[188:189]
	v_mfma_f32_16x16x32_bf16 v[64:67], v[76:79], v[2:5], v[64:67]
	v_mfma_f32_16x16x32_bf16 v[48:51], v[80:83], v[2:5], v[48:51]
	v_mfma_f32_16x16x32_bf16 v[40:43], v[60:63], v[2:5], v[40:43]
	v_mfma_f32_16x16x32_bf16 v[36:39], v[56:59], v[2:5], v[36:39]
	v_mfma_f32_16x16x32_bf16 v[144:147], v[88:91], v[2:5], v[30:33]
	v_mfma_f32_16x16x32_bf16 v[140:143], v[84:87], v[2:5], v[18:21]
	s_nop 1
	v_mov_b64_e32 v[32:33], v[212:213]
	v_mov_b64_e32 v[30:31], v[210:211]
	v_mov_b64_e32 v[14:15], v[182:183]
	s_waitcnt lgkmcnt(0)
	v_mfma_f32_16x16x32_bf16 v[148:151], v[72:75], v[2:5], v[22:25]
	v_mov_b64_e32 v[18:19], v[178:179]
	v_mov_b64_e32 v[20:21], v[180:181]
	v_mov_b64_e32 v[16:17], v[184:185]
	v_mfma_f32_16x16x32_bf16 v[152:155], v[68:71], v[2:5], v[6:9]
	v_mov_b64_e32 v[22:23], v[174:175]
	s_waitcnt vmcnt(0)
	v_mov_b64_e32 v[2:3], v[206:207]
	v_mov_b64_e32 v[24:25], v[176:177]
	v_mov_b64_e32 v[6:7], v[202:203]
	v_mov_b64_e32 v[8:9], v[204:205]
	v_mov_b64_e32 v[4:5], v[208:209]
	s_cbranch_scc1 .LBB0_2257
; __device__ __forceinline__ unsigned pk2(float lo, float hi) { return f2bf(lo) | (f2bf(hi) << 16); }
; template <int L>
; __device__ __forceinline__ void hyena_unit(CArgs& a, int l, int c, LAS unsigned char* lds) {
;     ...
;     for (int j = 0; j < NTW; ++j) *(u32x2*)(YT + 16 * (w * NTW + j) + 4 * kg) = (u32x2){pk2(acc[j][0], acc[j][1]), pk2(acc[j][2], acc[j][3])};
;     __syncthreads();
	v_lshlrev_b32_e32 v2, 8, v1
	v_cvt_pk_bf16_f32 v6, v148, v149
	v_lshl_add_u64 v[4:5], v[156:157], 0, v[34:35]
	v_cvt_pk_bf16_f32 v7, v150, v151
	v_ashrrev_i32_e32 v3, 31, v2
	v_lshl_add_u64 v[2:3], v[2:3], 1, v[4:5]
	s_mov_b64 s[14:15], 0x50400200
	v_lshl_add_u64 v[4:5], v[2:3], 0, s[14:15]
	s_mov_b32 s14, 0x50400000
	v_add_co_u32_e32 v2, vcc, s14, v2
	s_nop 0
	s_nop 0
	v_addc_co_u32_e32 v3, vcc, 0, v3, vcc
	global_store_dwordx2 v[2:3], v[6:7], off offset:512
	v_cvt_pk_bf16_f32 v2, v152, v153
	v_cvt_pk_bf16_f32 v3, v154, v155
	global_store_dwordx2 v[4:5], v[2:3], off offset:32
	v_cvt_pk_bf16_f32 v2, v144, v145
	v_cvt_pk_bf16_f32 v3, v146, v147
	global_store_dwordx2 v[4:5], v[2:3], off offset:64
	v_cvt_pk_bf16_f32 v2, v140, v141
	v_cvt_pk_bf16_f32 v3, v142, v143
	global_store_dwordx2 v[4:5], v[2:3], off offset:96
	v_cvt_pk_bf16_f32 v2, v136, v137
	v_cvt_pk_bf16_f32 v3, v138, v139
	global_store_dwordx2 v[4:5], v[2:3], off offset:128
	v_cvt_pk_bf16_f32 v2, v132, v133
	v_cvt_pk_bf16_f32 v3, v134, v135
	global_store_dwordx2 v[4:5], v[2:3], off offset:160
	v_cvt_pk_bf16_f32 v2, v128, v129
	v_cvt_pk_bf16_f32 v3, v130, v131
	global_store_dwordx2 v[4:5], v[2:3], off offset:192
	v_cvt_pk_bf16_f32 v2, v124, v125
	v_cvt_pk_bf16_f32 v3, v126, v127
	global_store_dwordx2 v[4:5], v[2:3], off offset:224
	v_cvt_pk_bf16_f32 v2, v120, v121
	v_cvt_pk_bf16_f32 v3, v122, v123
	global_store_dwordx2 v[4:5], v[2:3], off offset:256
	v_cvt_pk_bf16_f32 v2, v92, v93
	v_cvt_pk_bf16_f32 v3, v94, v95
	global_store_dwordx2 v[4:5], v[2:3], off offset:288
	v_cvt_pk_bf16_f32 v2, v64, v65
	v_cvt_pk_bf16_f32 v3, v66, v67
	global_store_dwordx2 v[4:5], v[2:3], off offset:320
	v_cvt_pk_bf16_f32 v2, v48, v49
	v_cvt_pk_bf16_f32 v3, v50, v51
	global_store_dwordx2 v[4:5], v[2:3], off offset:352
	v_cvt_pk_bf16_f32 v2, v40, v41
	v_cvt_pk_bf16_f32 v3, v42, v43
	global_store_dwordx2 v[4:5], v[2:3], off offset:384
	v_cvt_pk_bf16_f32 v2, v36, v37
	v_cvt_pk_bf16_f32 v3, v38, v39
	global_store_dwordx2 v[4:5], v[2:3], off offset:416
	v_cvt_pk_bf16_f32 v2, v52, v53
	v_cvt_pk_bf16_f32 v3, v54, v55
	global_store_dwordx2 v[4:5], v[2:3], off offset:448
	v_cvt_pk_bf16_f32 v2, v44, v45
	v_cvt_pk_bf16_f32 v1, v46, v46
	v_lshrrev_b32_e32 v1, 16, v1
	v_cvt_pk_bf16_f32 v3, v47, v47
	v_and_or_b32 v3, v3, s80, v1
	global_store_dwordx2 v[4:5], v[2:3], off offset:480
	s_barrier
	s_branch .LBB0_2061

; #define LAS __attribute__((address_space(3)))
; template <int L>
; __device__ __forceinline__ void hyena_unit(CArgs& a, int l, int c, LAS unsigned char* lds) {
;     ...
;         for (int ib = 0; ib < 8; ++ib) {
;             const bf16* zq = zp + 256 * (ib < 7 ? ib + 1 : 7);
; #pragma unroll
;             for (int ii = 0; ii < 8; ++ii) zn[ii] = *(const bf16x8*)(zq + 32 * ii);
; #pragma unroll
;             for (int ii = 0; ii < 8; ++ii) {
;                 A[(16 - 2 * ii) & 15] = *(const LAS bf16x8*)(ap + 64 * ii);
;                 A[(17 - 2 * ii) & 15] = *(const LAS bf16x8*)(ap + 64 * ii - 32);
; #pragma unroll
;                 for (int jj = 0; jj < 16; ++jj) { const int j = (jj + 2) & 15; acc[j] = __builtin_amdgcn_mfma_f32_16x16x32_bf16(A[(j + 16 - 2 * ii) & 15], zc[ii], acc[j], 0, 0, 0); }
;             }
;             ap += 512;
; #pragma unroll
;             for (int ii = 0; ii < 8; ++ii) zc[ii] = zn[ii];
;         }
.LBB0_2417:
	s_waitcnt vmcnt(1) lgkmcnt(1)
	s_nop 0
	v_mfma_f32_16x16x32_bf16 v[44:47], v[56:59], v[30:33], v[44:47]
	s_cmpk_lg_i32 s6, 0x800
	s_cselect_b32 s78, s6, 0x700
	v_lshl_add_u64 v[214:215], s[78:79], 1, v[158:159]
	global_load_dwordx4 v[210:213], v[214:215], off
	global_load_dwordx4 v[170:173], v[214:215], off offset:64
	global_load_dwordx4 v[174:177], v[214:215], off offset:128
	global_load_dwordx4 v[178:181], v[214:215], off offset:192
	global_load_dwordx4 v[182:185], v[214:215], off offset:256
	global_load_dwordx4 v[186:189], v[214:215], off offset:320
	global_load_dwordx4 v[202:205], v[214:215], off offset:384
	global_load_dwordx4 v[206:209], v[214:215], off offset:448
	s_addk_i32 s6, 0x100
	v_mfma_f32_16x16x32_bf16 v[36:39], v[80:83], v[30:33], v[36:39]
	s_cmpk_lg_i32 s6, 0x900
	v_mfma_f32_16x16x32_bf16 v[44:47], v[80:83], v[26:29], v[44:47]
	v_mfma_f32_16x16x32_bf16 v[136:139], v[88:91], v[30:33], v[136:139]
	v_mfma_f32_16x16x32_bf16 v[132:135], v[84:87], v[30:33], v[132:135]
	v_mfma_f32_16x16x32_bf16 v[128:131], v[104:107], v[30:33], v[128:131]
	v_mfma_f32_16x16x32_bf16 v[124:127], v[96:99], v[30:33], v[124:127]
	v_mfma_f32_16x16x32_bf16 v[48:51], v[112:115], v[30:33], v[48:51]
	v_mfma_f32_16x16x32_bf16 v[36:39], v[112:115], v[26:29], v[36:39]
	v_mfma_f32_16x16x32_bf16 v[44:47], v[112:115], v[22:25], v[44:47]
	v_subrev_u32_e32 v112, 32, v161
	s_waitcnt lgkmcnt(0)
	v_mfma_f32_16x16x32_bf16 v[52:55], v[60:63], v[30:33], v[52:55]
	v_mfma_f32_16x16x32_bf16 v[56:59], v[72:75], v[26:29], v[136:139]
	v_mfma_f32_16x16x32_bf16 v[60:63], v[68:71], v[26:29], v[132:135]
	s_nop 1
	ds_read_b128 v[136:139], v112
	ds_read_b128 v[132:135], v161
	v_mfma_f32_16x16x32_bf16 v[128:131], v[88:91], v[26:29], v[128:131]
	v_mfma_f32_16x16x32_bf16 v[124:127], v[84:87], v[26:29], v[124:127]
	v_mfma_f32_16x16x32_bf16 v[140:143], v[68:71], v[30:33], v[140:143]
	v_mfma_f32_16x16x32_bf16 v[40:43], v[76:79], v[30:33], v[40:43]
	v_mfma_f32_16x16x32_bf16 v[52:55], v[76:79], v[26:29], v[52:55]
	v_mfma_f32_16x16x32_bf16 v[76:79], v[72:75], v[22:25], v[128:131]
	v_mfma_f32_16x16x32_bf16 v[80:83], v[68:71], v[22:25], v[124:127]
	v_mfma_f32_16x16x32_bf16 v[144:147], v[72:75], v[30:33], v[144:147]
	s_waitcnt lgkmcnt(0)
	v_mfma_f32_16x16x32_bf16 v[124:127], v[132:135], v[22:25], v[56:59]
	v_mfma_f32_16x16x32_bf16 v[128:131], v[136:139], v[26:29], v[140:143]
	v_mfma_f32_16x16x32_bf16 v[140:143], v[136:139], v[22:25], v[60:63]
	s_nop 2
	ds_read_b128 v[60:63], v161 offset:64
	ds_read_b128 v[56:59], v161 offset:32
	v_mfma_f32_16x16x32_bf16 v[120:123], v[100:103], v[30:33], v[120:123]
	v_mfma_f32_16x16x32_bf16 v[92:95], v[108:111], v[30:33], v[92:95]
	v_mfma_f32_16x16x32_bf16 v[64:67], v[116:119], v[30:33], v[64:67]
	v_mfma_f32_16x16x32_bf16 v[40:43], v[116:119], v[26:29], v[40:43]
	v_mfma_f32_16x16x32_bf16 v[52:55], v[116:119], v[22:25], v[52:55]
	v_mfma_f32_16x16x32_bf16 v[112:115], v[132:135], v[30:33], v[148:151]
	v_mfma_f32_16x16x32_bf16 v[30:33], v[136:139], v[30:33], v[152:155]
	v_mfma_f32_16x16x32_bf16 v[76:79], v[132:135], v[18:21], v[76:79]
	v_mfma_f32_16x16x32_bf16 v[80:83], v[136:139], v[18:21], v[80:83]
	v_mfma_f32_16x16x32_bf16 v[116:119], v[132:135], v[26:29], v[144:147]
	v_mfma_f32_16x16x32_bf16 v[120:123], v[104:107], v[26:29], v[120:123]
	v_mfma_f32_16x16x32_bf16 v[92:95], v[96:99], v[26:29], v[92:95]
	v_mfma_f32_16x16x32_bf16 v[64:67], v[100:103], v[26:29], v[64:67]
	v_mfma_f32_16x16x32_bf16 v[48:51], v[108:111], v[26:29], v[48:51]
	v_mfma_f32_16x16x32_bf16 v[40:43], v[100:103], v[22:25], v[40:43]
	v_mfma_f32_16x16x32_bf16 v[52:55], v[100:103], v[18:21], v[52:55]
	s_waitcnt lgkmcnt(1)
	v_mfma_f32_16x16x32_bf16 v[100:103], v[60:63], v[26:29], v[112:115]
	v_mfma_f32_16x16x32_bf16 v[112:115], v[60:63], v[18:21], v[124:127]
	s_waitcnt lgkmcnt(0)
	v_mfma_f32_16x16x32_bf16 v[26:29], v[56:59], v[26:29], v[30:33]
	v_mfma_f32_16x16x32_bf16 v[30:33], v[56:59], v[22:25], v[128:131]
	v_mfma_f32_16x16x32_bf16 v[124:127], v[60:63], v[14:17], v[76:79]
	v_mfma_f32_16x16x32_bf16 v[128:131], v[56:59], v[14:17], v[80:83]
	s_nop 1
	ds_read_b128 v[76:79], v161 offset:128
	ds_read_b128 v[80:83], v161 offset:96
	v_mfma_f32_16x16x32_bf16 v[36:39], v[108:111], v[22:25], v[36:39]
	v_mfma_f32_16x16x32_bf16 v[44:47], v[108:111], v[18:21], v[44:47]
	v_mfma_f32_16x16x32_bf16 v[108:111], v[60:63], v[22:25], v[116:119]
	v_mfma_f32_16x16x32_bf16 v[116:119], v[56:59], v[18:21], v[140:143]
	v_mfma_f32_16x16x32_bf16 v[120:123], v[88:91], v[22:25], v[120:123]
	v_mfma_f32_16x16x32_bf16 v[92:95], v[84:87], v[22:25], v[92:95]
	v_mfma_f32_16x16x32_bf16 v[64:67], v[104:107], v[22:25], v[64:67]
	v_mfma_f32_16x16x32_bf16 v[48:51], v[96:99], v[22:25], v[48:51]
	v_mfma_f32_16x16x32_bf16 v[40:43], v[104:107], v[18:21], v[40:43]
	v_mfma_f32_16x16x32_bf16 v[36:39], v[96:99], v[18:21], v[36:39]
	v_mfma_f32_16x16x32_bf16 v[52:55], v[104:107], v[14:17], v[52:55]
	v_mfma_f32_16x16x32_bf16 v[44:47], v[96:99], v[14:17], v[44:47]
	s_waitcnt lgkmcnt(1)
	v_mfma_f32_16x16x32_bf16 v[96:99], v[76:79], v[22:25], v[100:103]
	v_mfma_f32_16x16x32_bf16 v[104:107], v[76:79], v[14:17], v[112:115]
	s_waitcnt lgkmcnt(0)
; #define LAS __attribute__((address_space(3)))
; template <int L>
; __device__ __forceinline__ void hyena_unit(CArgs& a, int l, int c, LAS unsigned char* lds) {
;     ...
;         for (int ib = 0; ib < 8; ++ib) {
;             const bf16* zq = zp + 256 * (ib < 7 ? ib + 1 : 7);
; #pragma unroll
;             for (int ii = 0; ii < 8; ++ii) zn[ii] = *(const bf16x8*)(zq + 32 * ii);
; #pragma unroll
;             for (int ii = 0; ii < 8; ++ii) {
;                 A[(16 - 2 * ii) & 15] = *(const LAS bf16x8*)(ap + 64 * ii);
;                 A[(17 - 2 * ii) & 15] = *(const LAS bf16x8*)(ap + 64 * ii - 32);
; #pragma unroll
;                 for (int jj = 0; jj < 16; ++jj) { const int j = (jj + 2) & 15; acc[j] = __builtin_amdgcn_mfma_f32_16x16x32_bf16(A[(j + 16 - 2 * ii) & 15], zc[ii], acc[j], 0, 0, 0); }
;             }
;             ap += 512;
; #pragma unroll
;             for (int ii = 0; ii < 8; ++ii) zc[ii] = zn[ii];
;         }
	v_mfma_f32_16x16x32_bf16 v[22:25], v[80:83], v[22:25], v[26:29]
	v_mfma_f32_16x16x32_bf16 v[26:29], v[80:83], v[18:21], v[30:33]
	v_mfma_f32_16x16x32_bf16 v[30:33], v[80:83], v[14:17], v[116:119]
	s_nop 2
	ds_read_b128 v[116:119], v161 offset:192
	ds_read_b128 v[112:115], v161 offset:160
	v_mfma_f32_16x16x32_bf16 v[100:103], v[76:79], v[18:21], v[108:111]
	v_mfma_f32_16x16x32_bf16 v[108:111], v[76:79], v[10:13], v[124:127]
	v_mfma_f32_16x16x32_bf16 v[124:127], v[80:83], v[10:13], v[128:131]
	v_mfma_f32_16x16x32_bf16 v[120:123], v[72:75], v[18:21], v[120:123]
	v_mfma_f32_16x16x32_bf16 v[92:95], v[68:71], v[18:21], v[92:95]
	v_mfma_f32_16x16x32_bf16 v[64:67], v[88:91], v[18:21], v[64:67]
	v_mfma_f32_16x16x32_bf16 v[48:51], v[84:87], v[18:21], v[48:51]
	v_mfma_f32_16x16x32_bf16 v[40:43], v[88:91], v[14:17], v[40:43]
	v_mfma_f32_16x16x32_bf16 v[36:39], v[84:87], v[14:17], v[36:39]
	v_mfma_f32_16x16x32_bf16 v[52:55], v[88:91], v[10:13], v[52:55]
	v_mfma_f32_16x16x32_bf16 v[44:47], v[84:87], v[10:13], v[44:47]
	s_waitcnt lgkmcnt(1)
	v_mfma_f32_16x16x32_bf16 v[84:87], v[116:119], v[18:21], v[96:99]
	v_mfma_f32_16x16x32_bf16 v[88:91], v[116:119], v[14:17], v[100:103]
	s_waitcnt lgkmcnt(0)
	v_mfma_f32_16x16x32_bf16 v[18:21], v[112:115], v[18:21], v[22:25]
	v_mfma_f32_16x16x32_bf16 v[22:25], v[112:115], v[14:17], v[26:29]
	v_mfma_f32_16x16x32_bf16 v[26:29], v[112:115], v[10:13], v[30:33]
	v_mfma_f32_16x16x32_bf16 v[30:33], v[116:119], v[6:9], v[108:111]
	ds_read_b128 v[100:103], v161 offset:256
	s_nop 1
	ds_read_b128 v[108:111], v161 offset:224
	v_mfma_f32_16x16x32_bf16 v[96:99], v[116:119], v[10:13], v[104:107]
	v_mfma_f32_16x16x32_bf16 v[104:107], v[112:115], v[6:9], v[124:127]
	v_mfma_f32_16x16x32_bf16 v[48:51], v[68:71], v[14:17], v[48:51]
	v_mfma_f32_16x16x32_bf16 v[36:39], v[68:71], v[10:13], v[36:39]
	v_mfma_f32_16x16x32_bf16 v[44:47], v[68:71], v[6:9], v[44:47]
	s_waitcnt lgkmcnt(1)
	v_mfma_f32_16x16x32_bf16 v[68:71], v[100:103], v[14:17], v[84:87]
	v_mfma_f32_16x16x32_bf16 v[84:87], v[100:103], v[6:9], v[96:99]
	s_waitcnt vmcnt(8) lgkmcnt(0)
	v_mfma_f32_16x16x32_bf16 v[124:127], v[108:111], v[2:5], v[104:107]
	s_nop 2
	ds_read_b128 v[104:107], v161 offset:320
	ds_read_b128 v[96:99], v161 offset:288
	v_mfma_f32_16x16x32_bf16 v[120:123], v[132:135], v[14:17], v[120:123]
	v_mfma_f32_16x16x32_bf16 v[92:95], v[136:139], v[14:17], v[92:95]
	v_mfma_f32_16x16x32_bf16 v[64:67], v[72:75], v[14:17], v[64:67]
	v_mfma_f32_16x16x32_bf16 v[14:17], v[108:111], v[14:17], v[18:21]
	v_mfma_f32_16x16x32_bf16 v[18:21], v[108:111], v[10:13], v[22:25]
	v_mfma_f32_16x16x32_bf16 v[22:25], v[108:111], v[6:9], v[26:29]
	s_waitcnt lgkmcnt(1)
	v_mfma_f32_16x16x32_bf16 v[26:29], v[104:107], v[10:13], v[68:71]
	s_nop 2
	v_mfma_f32_16x16x32_bf16 v[120:123], v[60:63], v[10:13], v[120:123]
	v_mfma_f32_16x16x32_bf16 v[92:95], v[56:59], v[10:13], v[92:95]
	v_mfma_f32_16x16x32_bf16 v[64:67], v[132:135], v[10:13], v[64:67]
	v_mfma_f32_16x16x32_bf16 v[48:51], v[136:139], v[10:13], v[48:51]
	v_mfma_f32_16x16x32_bf16 v[40:43], v[72:75], v[10:13], v[40:43]
	v_mfma_f32_16x16x32_bf16 v[52:55], v[72:75], v[6:9], v[52:55]
	v_mfma_f32_16x16x32_bf16 v[72:75], v[100:103], v[10:13], v[88:91]
	s_waitcnt lgkmcnt(0)
	v_mfma_f32_16x16x32_bf16 v[10:13], v[96:99], v[10:13], v[14:17]
	s_nop 2
	v_mfma_f32_16x16x32_bf16 v[36:39], v[136:139], v[6:9], v[36:39]
	v_mfma_f32_16x16x32_bf16 v[44:47], v[136:139], v[2:5], v[44:47]
	v_mfma_f32_16x16x32_bf16 v[136:139], v[104:107], v[2:5], v[84:87]
	ds_read_b128 v[88:91], v161 offset:384
	s_nop 1
	ds_read_b128 v[84:87], v161 offset:352
	v_mfma_f32_16x16x32_bf16 v[128:131], v[100:103], v[2:5], v[30:33]
	ds_read_b128 v[68:71], v161 offset:416
	v_mfma_f32_16x16x32_bf16 v[30:33], v[104:107], v[6:9], v[72:75]
	s_nop 2
	ds_read_b128 v[72:75], v161 offset:448
	v_mfma_f32_16x16x32_bf16 v[120:123], v[76:79], v[6:9], v[120:123]
	v_add_u32_e32 v161, 0x200, v161
	v_mfma_f32_16x16x32_bf16 v[92:95], v[80:83], v[6:9], v[92:95]
	v_mfma_f32_16x16x32_bf16 v[64:67], v[60:63], v[6:9], v[64:67]
	v_mfma_f32_16x16x32_bf16 v[48:51], v[56:59], v[6:9], v[48:51]
	v_mfma_f32_16x16x32_bf16 v[40:43], v[132:135], v[6:9], v[40:43]
	v_mfma_f32_16x16x32_bf16 v[52:55], v[132:135], v[2:5], v[52:55]
	v_mfma_f32_16x16x32_bf16 v[18:21], v[96:99], v[6:9], v[18:21]
	v_mfma_f32_16x16x32_bf16 v[132:135], v[96:99], v[2:5], v[22:25]
	s_waitcnt lgkmcnt(3)
	v_mfma_f32_16x16x32_bf16 v[22:25], v[88:91], v[6:9], v[26:29]
	s_waitcnt lgkmcnt(2)
	v_mfma_f32_16x16x32_bf16 v[6:9], v[84:87], v[6:9], v[10:13]
	s_waitcnt vmcnt(6)
	v_mov_b64_e32 v[26:27], v[170:171]
	v_mfma_f32_16x16x32_bf16 v[120:123], v[116:119], v[2:5], v[120:123]
	v_mov_b64_e32 v[28:29], v[172:173]
	s_waitcnt vmcnt(2)
	v_mov_b64_e32 v[10:11], v[186:187]
	v_mfma_f32_16x16x32_bf16 v[92:95], v[112:115], v[2:5], v[92:95]
	v_mov_b64_e32 v[12:13], v[188:189]
	v_mfma_f32_16x16x32_bf16 v[64:67], v[76:79], v[2:5], v[64:67]
	v_mfma_f32_16x16x32_bf16 v[48:51], v[80:83], v[2:5], v[48:51]
	v_mfma_f32_16x16x32_bf16 v[40:43], v[60:63], v[2:5], v[40:43]
	v_mfma_f32_16x16x32_bf16 v[36:39], v[56:59], v[2:5], v[36:39]
	v_mfma_f32_16x16x32_bf16 v[144:147], v[88:91], v[2:5], v[30:33]
	v_mfma_f32_16x16x32_bf16 v[140:143], v[84:87], v[2:5], v[18:21]
	s_nop 1
	v_mov_b64_e32 v[32:33], v[212:213]
	v_mov_b64_e32 v[30:31], v[210:211]
	v_mov_b64_e32 v[14:15], v[182:183]
	s_waitcnt lgkmcnt(0)
	v_mfma_f32_16x16x32_bf16 v[148:151], v[72:75], v[2:5], v[22:25]
	v_mov_b64_e32 v[18:19], v[178:179]
	v_mov_b64_e32 v[20:21], v[180:181]
	v_mov_b64_e32 v[16:17], v[184:185]
	v_mfma_f32_16x16x32_bf16 v[152:155], v[68:71], v[2:5], v[6:9]
	v_mov_b64_e32 v[22:23], v[174:175]
	s_waitcnt vmcnt(0)
	v_mov_b64_e32 v[2:3], v[206:207]
	v_mov_b64_e32 v[24:25], v[176:177]
	v_mov_b64_e32 v[6:7], v[202:203]
	v_mov_b64_e32 v[8:9], v[204:205]
	v_mov_b64_e32 v[4:5], v[208:209]
	s_cbranch_scc1 .LBB0_2417
; #define LAS __attribute__((address_space(3)))
; __device__ __forceinline__ unsigned pk2(float lo, float hi) { return f2bf(lo) | (f2bf(hi) << 16); }
; template <int L>
; __device__ __forceinline__ void hyena_unit(CArgs& a, int l, int c, LAS unsigned char* lds) {
;     ...
;     const float* kf = (const float*)(a.ws + WS_KUN) + ((size_t)((l * 2 + Lt) * 512 + c)) * 2048;
;     const float* kb = kf + (size_t)256 * 2048;
;     LAS float* red = (LAS float*)(lds + 8 * CST);
;     const bf16* Z = (const bf16*)(a.ws + WS_MIX + MX_ZT) + ((size_t)(c * 16 + fr)) * 2304 + SOFF;
;     const bf16* zp = Z + 8 * kg;
;     bf16x8 zc[8];
; #pragma unroll
;     for (int ii = 0; ii < 8; ++ii) zc[ii] = *(const bf16x8*)(zp + 32 * ii);
;     constexpr int NI = (2 * L + 16 + 511) / 512;
;     float gv[NI];
;     float s = 0.f;
; #pragma unroll
;     for (int q = 0; q < NI; ++q) {
;         const int idx = tid + 512 * q, ic = min(max(idx, 1), 2 * L - 1);
;         const float v = *(ic <= L ? kf + (L - ic) : kb + (ic - L));
;         gv[q] = (idx >= 1 && idx < 2 * L) ? v : 0.f;
;         s += fabsf(gv[q]);
;     }
;     s = wave_sum(s);
;     if (lane == 0) red[w] = s;
;     ...
;     for (int j = 0; j < NTW; ++j) *(u32x2*)(YT + 16 * (w * NTW + j) + 4 * kg) = (u32x2){pk2(acc[j][0], acc[j][1]), pk2(acc[j][2], acc[j][3])};
;     __syncthreads();
	v_lshlrev_b32_e32 v2, 8, v1
	v_cvt_pk_bf16_f32 v6, v148, v149
	v_lshl_add_u64 v[4:5], v[156:157], 0, v[34:35]
	v_cvt_pk_bf16_f32 v7, v150, v151
	v_ashrrev_i32_e32 v3, 31, v2
	v_lshl_add_u64 v[2:3], v[2:3], 1, v[4:5]
	s_mov_b64 s[6:7], 0x50400200
	v_lshl_add_u64 v[4:5], v[2:3], 0, s[6:7]
	s_mov_b32 s6, 0x50400000
	v_add_co_u32_e32 v2, vcc, s6, v2
	s_nop 0
	s_nop 0
	v_addc_co_u32_e32 v3, vcc, 0, v3, vcc
	global_store_dwordx2 v[2:3], v[6:7], off offset:512
	v_cvt_pk_bf16_f32 v2, v152, v153
	v_cvt_pk_bf16_f32 v3, v154, v155
	global_store_dwordx2 v[4:5], v[2:3], off offset:32
	v_cvt_pk_bf16_f32 v2, v144, v145
	v_cvt_pk_bf16_f32 v3, v146, v147
	global_store_dwordx2 v[4:5], v[2:3], off offset:64
	v_cvt_pk_bf16_f32 v2, v140, v141
	v_cvt_pk_bf16_f32 v3, v142, v143
	global_store_dwordx2 v[4:5], v[2:3], off offset:96
	v_cvt_pk_bf16_f32 v2, v136, v137
	v_cvt_pk_bf16_f32 v3, v138, v139
	global_store_dwordx2 v[4:5], v[2:3], off offset:128
	v_cvt_pk_bf16_f32 v2, v132, v133
	v_cvt_pk_bf16_f32 v3, v134, v135
	global_store_dwordx2 v[4:5], v[2:3], off offset:160
	v_cvt_pk_bf16_f32 v2, v128, v129
	v_cvt_pk_bf16_f32 v3, v130, v131
	global_store_dwordx2 v[4:5], v[2:3], off offset:192
	v_cvt_pk_bf16_f32 v2, v124, v125
	v_cvt_pk_bf16_f32 v3, v126, v127
	global_store_dwordx2 v[4:5], v[2:3], off offset:224
	v_cvt_pk_bf16_f32 v2, v120, v121
	v_cvt_pk_bf16_f32 v3, v122, v123
	global_store_dwordx2 v[4:5], v[2:3], off offset:256
	v_cvt_pk_bf16_f32 v2, v92, v93
	v_cvt_pk_bf16_f32 v3, v94, v95
	global_store_dwordx2 v[4:5], v[2:3], off offset:288
	v_cvt_pk_bf16_f32 v2, v64, v65
	v_cvt_pk_bf16_f32 v3, v66, v67
	global_store_dwordx2 v[4:5], v[2:3], off offset:320
	v_cvt_pk_bf16_f32 v2, v48, v49
	v_cvt_pk_bf16_f32 v3, v50, v51
	global_store_dwordx2 v[4:5], v[2:3], off offset:352
	v_cvt_pk_bf16_f32 v2, v40, v41
	v_cvt_pk_bf16_f32 v3, v42, v43
	global_store_dwordx2 v[4:5], v[2:3], off offset:384
	v_cvt_pk_bf16_f32 v2, v36, v37
	v_cvt_pk_bf16_f32 v3, v38, v39
	global_store_dwordx2 v[4:5], v[2:3], off offset:416
	v_cvt_pk_bf16_f32 v2, v52, v53
	v_cvt_pk_bf16_f32 v3, v54, v55
	global_store_dwordx2 v[4:5], v[2:3], off offset:448
	v_cvt_pk_bf16_f32 v2, v44, v45
	v_cvt_pk_bf16_f32 v1, v46, v46
	v_readlane_b32 s10, v250, 58
	v_lshrrev_b32_e32 v1, 16, v1
	v_cvt_pk_bf16_f32 v3, v47, v47
	v_readlane_b32 s11, v250, 59
	v_and_or_b32 v3, v3, s80, v1
	s_mov_b64 s[6:7], 0
	s_andn2_b64 vcc, exec, s[10:11]
	s_mov_b64 s[14:15], 0
	global_store_dwordx2 v[4:5], v[2:3], off offset:480
	s_barrier
	s_cbranch_vccnz .LBB0_2494
	v_readlane_b32 s9, v252, 21
	s_add_i32 s10, s8, s9
	v_mov_b32_e32 v38, v0
	s_ashr_i32 s11, s10, 31
	s_lshl_b64 s[10:11], s[10:11], 13
	v_and_b32_e32 v39, 15, v38
	v_readlane_b32 s9, v252, 22
	s_add_u32 s26, s2, 0x4f000000
	s_addc_u32 s27, s3, 0
	v_or_b32_e32 v1, s9, v39
	s_movk_i32 s9, 0x900
	v_mad_u64_u32 v[36:37], s[14:15], v1, s9, 0
	v_lshl_add_u64 v[2:3], v[36:37], 1, s[26:27]
	v_and_b32_e32 v34, 48, v38
	s_add_u32 s10, s0, s10
	v_med3_i32 v1, v38, 1, v197
	v_lshl_add_u64 v[2:3], v[2:3], 0, v[34:35]
	s_addc_u32 s11, s1, s11
	v_sub_u32_e32 v34, 0x100, v1
	v_lshl_add_u64 v[4:5], v[34:35], 2, s[10:11]
	v_lshlrev_b32_e32 v34, 2, v1
	v_lshl_add_u64 v[6:7], s[10:11], 0, v[34:35]
	s_mov_b64 s[14:15], 0x1ffc00
	s_movk_i32 s9, 0x101
	v_lshl_add_u64 v[6:7], v[6:7], 0, s[14:15]
	v_cmp_gt_i32_e32 vcc, s9, v38
	v_add_u32_e32 v40, 0x200, v38
	v_med3_i32 v1, v40, 1, v197
	v_cndmask_b32_e32 v5, v7, v5, vcc
	v_cndmask_b32_e32 v4, v6, v4, vcc
	global_load_dword v41, v[4:5], off
	v_sub_u32_e32 v34, 0x100, v1
	v_lshl_add_u64 v[4:5], v[34:35], 2, s[10:11]
	v_lshlrev_b32_e32 v34, 2, v1
	v_lshl_add_u64 v[6:7], s[10:11], 0, v[34:35]
	s_movk_i32 s9, 0xff01
	v_lshl_add_u64 v[6:7], v[6:7], 0, s[14:15]
	v_cmp_gt_i32_e32 vcc, s9, v38
	v_add_u32_e32 v34, -1, v38
	s_movk_i32 s9, 0x1ff
	v_cndmask_b32_e32 v5, v7, v5, vcc
	v_cndmask_b32_e32 v4, v6, v4, vcc
	global_load_dword v42, v[4:5], off
	global_load_dwordx4 v[30:33], v[2:3], off
	global_load_dwordx4 v[26:29], v[2:3], off offset:64
	global_load_dwordx4 v[22:25], v[2:3], off offset:128
	global_load_dwordx4 v[18:21], v[2:3], off offset:192
	global_load_dwordx4 v[14:17], v[2:3], off offset:256
	global_load_dwordx4 v[10:13], v[2:3], off offset:320
	global_load_dwordx4 v[6:9], v[2:3], off offset:384
	s_nop 0
	global_load_dwordx4 v[2:5], v[2:3], off offset:448
	v_cmp_gt_u32_e32 vcc, s9, v34
	v_and_b32_e32 v43, 63, v38
	v_ashrrev_i32_e32 v1, 6, v38
	s_waitcnt vmcnt(9)
	v_cndmask_b32_e32 v34, 0, v41, vcc
	v_cmp_lt_u32_e32 vcc, s30, v38
	s_waitcnt vmcnt(8)
	s_nop 0
	v_cndmask_b32_e32 v41, 0, v42, vcc
	v_add_f32_e64 v42, |v34|, |v41|
	v_cmp_eq_u32_e32 vcc, 0, v43
	s_nop 0
	v_add_f32_dpp v42, v42, v42 quad_perm:[1,0,3,2] row_mask:0xf bank_mask:0xf bound_ctrl:1
	s_nop 1
	v_add_f32_dpp v42, v42, v42 quad_perm:[2,3,0,1] row_mask:0xf bank_mask:0xf bound_ctrl:1
	s_nop 1
	v_add_f32_dpp v42, v42, v42 row_half_mirror row_mask:0xf bank_mask:0xf bound_ctrl:1
	s_nop 1
	v_add_f32_dpp v42, v42, v42 row_mirror row_mask:0xf bank_mask:0xf bound_ctrl:1
	s_nop 0
	v_readlane_b32 s28, v42, 0
	v_readlane_b32 s9, v42, 16
	v_readlane_b32 s29, v42, 32
	v_readlane_b32 s10, v42, 48
	s_and_saveexec_b64 s[14:15], vcc
	s_cbranch_execz .LBB0_2421
	v_mov_b32_e32 v42, s9
	v_mov_b32_e32 v43, s10
	v_pk_add_f32 v[42:43], s[28:29], v[42:43]
	v_lshl_add_u32 v44, v1, 2, 0
	v_add_f32_e32 v42, v42, v43
	ds_write_b32 v44, v42 offset:8704

; #define LAS __attribute__((address_space(3)))
; template <int L>
; __device__ __forceinline__ void hyena_unit(CArgs& a, int l, int c, LAS unsigned char* lds) {
;     ...
;         for (int ib = 0; ib < 8; ++ib) {
;             const bf16* zq = zp + 256 * (ib < 7 ? ib + 1 : 7);
; #pragma unroll
;             for (int ii = 0; ii < 8; ++ii) zn[ii] = *(const bf16x8*)(zq + 32 * ii);
; #pragma unroll
;             for (int ii = 0; ii < 8; ++ii) {
;                 A[(16 - 2 * ii) & 15] = *(const LAS bf16x8*)(ap + 64 * ii);
;                 A[(17 - 2 * ii) & 15] = *(const LAS bf16x8*)(ap + 64 * ii - 32);
; #pragma unroll
;                 for (int jj = 0; jj < 16; ++jj) { const int j = (jj + 2) & 15; acc[j] = __builtin_amdgcn_mfma_f32_16x16x32_bf16(A[(j + 16 - 2 * ii) & 15], zc[ii], acc[j], 0, 0, 0); }
;             }
;             ap += 512;
; #pragma unroll
;             for (int ii = 0; ii < 8; ++ii) zc[ii] = zn[ii];
;         }
.LBB0_2649:
	s_waitcnt vmcnt(1) lgkmcnt(1)
	s_nop 0
	v_mfma_f32_16x16x32_bf16 v[44:47], v[56:59], v[30:33], v[44:47]
	s_cmpk_lg_i32 s0, 0x800
	s_cselect_b32 s78, s0, 0x700
	v_lshl_add_u64 v[214:215], s[78:79], 1, v[158:159]
	global_load_dwordx4 v[210:213], v[214:215], off
	global_load_dwordx4 v[170:173], v[214:215], off offset:64
	global_load_dwordx4 v[174:177], v[214:215], off offset:128
	global_load_dwordx4 v[178:181], v[214:215], off offset:192
	global_load_dwordx4 v[182:185], v[214:215], off offset:256
	global_load_dwordx4 v[186:189], v[214:215], off offset:320
	global_load_dwordx4 v[202:205], v[214:215], off offset:384
	global_load_dwordx4 v[206:209], v[214:215], off offset:448
	s_addk_i32 s0, 0x100
	v_mfma_f32_16x16x32_bf16 v[36:39], v[80:83], v[30:33], v[36:39]
	s_cmpk_lg_i32 s0, 0x900
	v_mfma_f32_16x16x32_bf16 v[44:47], v[80:83], v[26:29], v[44:47]
	v_mfma_f32_16x16x32_bf16 v[136:139], v[88:91], v[30:33], v[136:139]
	v_mfma_f32_16x16x32_bf16 v[132:135], v[84:87], v[30:33], v[132:135]
	v_mfma_f32_16x16x32_bf16 v[128:131], v[104:107], v[30:33], v[128:131]
	v_mfma_f32_16x16x32_bf16 v[124:127], v[96:99], v[30:33], v[124:127]
	v_mfma_f32_16x16x32_bf16 v[48:51], v[112:115], v[30:33], v[48:51]
	v_mfma_f32_16x16x32_bf16 v[36:39], v[112:115], v[26:29], v[36:39]
	v_mfma_f32_16x16x32_bf16 v[44:47], v[112:115], v[22:25], v[44:47]
	v_subrev_u32_e32 v112, 32, v161
	s_waitcnt lgkmcnt(0)
	v_mfma_f32_16x16x32_bf16 v[52:55], v[60:63], v[30:33], v[52:55]
	v_mfma_f32_16x16x32_bf16 v[56:59], v[72:75], v[26:29], v[136:139]
	v_mfma_f32_16x16x32_bf16 v[60:63], v[68:71], v[26:29], v[132:135]
	s_nop 1
	ds_read_b128 v[136:139], v112
	ds_read_b128 v[132:135], v161
	v_mfma_f32_16x16x32_bf16 v[128:131], v[88:91], v[26:29], v[128:131]
	v_mfma_f32_16x16x32_bf16 v[124:127], v[84:87], v[26:29], v[124:127]
	v_mfma_f32_16x16x32_bf16 v[140:143], v[68:71], v[30:33], v[140:143]
	v_mfma_f32_16x16x32_bf16 v[40:43], v[76:79], v[30:33], v[40:43]
	v_mfma_f32_16x16x32_bf16 v[52:55], v[76:79], v[26:29], v[52:55]
	v_mfma_f32_16x16x32_bf16 v[76:79], v[72:75], v[22:25], v[128:131]
	v_mfma_f32_16x16x32_bf16 v[80:83], v[68:71], v[22:25], v[124:127]
	v_mfma_f32_16x16x32_bf16 v[144:147], v[72:75], v[30:33], v[144:147]
	s_waitcnt lgkmcnt(0)
	v_mfma_f32_16x16x32_bf16 v[124:127], v[132:135], v[22:25], v[56:59]
	v_mfma_f32_16x16x32_bf16 v[128:131], v[136:139], v[26:29], v[140:143]
	v_mfma_f32_16x16x32_bf16 v[140:143], v[136:139], v[22:25], v[60:63]
	s_nop 2
	ds_read_b128 v[60:63], v161 offset:64
	ds_read_b128 v[56:59], v161 offset:32
	v_mfma_f32_16x16x32_bf16 v[120:123], v[100:103], v[30:33], v[120:123]
	v_mfma_f32_16x16x32_bf16 v[92:95], v[108:111], v[30:33], v[92:95]
	v_mfma_f32_16x16x32_bf16 v[64:67], v[116:119], v[30:33], v[64:67]
	v_mfma_f32_16x16x32_bf16 v[40:43], v[116:119], v[26:29], v[40:43]
	v_mfma_f32_16x16x32_bf16 v[52:55], v[116:119], v[22:25], v[52:55]
	v_mfma_f32_16x16x32_bf16 v[112:115], v[132:135], v[30:33], v[148:151]
	v_mfma_f32_16x16x32_bf16 v[30:33], v[136:139], v[30:33], v[152:155]
	v_mfma_f32_16x16x32_bf16 v[76:79], v[132:135], v[18:21], v[76:79]
	v_mfma_f32_16x16x32_bf16 v[80:83], v[136:139], v[18:21], v[80:83]
	v_mfma_f32_16x16x32_bf16 v[116:119], v[132:135], v[26:29], v[144:147]
	v_mfma_f32_16x16x32_bf16 v[120:123], v[104:107], v[26:29], v[120:123]
	v_mfma_f32_16x16x32_bf16 v[92:95], v[96:99], v[26:29], v[92:95]
	v_mfma_f32_16x16x32_bf16 v[64:67], v[100:103], v[26:29], v[64:67]
	v_mfma_f32_16x16x32_bf16 v[48:51], v[108:111], v[26:29], v[48:51]
	v_mfma_f32_16x16x32_bf16 v[40:43], v[100:103], v[22:25], v[40:43]
	v_mfma_f32_16x16x32_bf16 v[52:55], v[100:103], v[18:21], v[52:55]
	s_waitcnt lgkmcnt(1)
	v_mfma_f32_16x16x32_bf16 v[100:103], v[60:63], v[26:29], v[112:115]
	v_mfma_f32_16x16x32_bf16 v[112:115], v[60:63], v[18:21], v[124:127]
	s_waitcnt lgkmcnt(0)
	v_mfma_f32_16x16x32_bf16 v[26:29], v[56:59], v[26:29], v[30:33]
	v_mfma_f32_16x16x32_bf16 v[30:33], v[56:59], v[22:25], v[128:131]
	v_mfma_f32_16x16x32_bf16 v[124:127], v[60:63], v[14:17], v[76:79]
	v_mfma_f32_16x16x32_bf16 v[128:131], v[56:59], v[14:17], v[80:83]
	s_nop 1
	ds_read_b128 v[76:79], v161 offset:128
	ds_read_b128 v[80:83], v161 offset:96
	v_mfma_f32_16x16x32_bf16 v[36:39], v[108:111], v[22:25], v[36:39]
	v_mfma_f32_16x16x32_bf16 v[44:47], v[108:111], v[18:21], v[44:47]
	v_mfma_f32_16x16x32_bf16 v[108:111], v[60:63], v[22:25], v[116:119]
	v_mfma_f32_16x16x32_bf16 v[116:119], v[56:59], v[18:21], v[140:143]
	v_mfma_f32_16x16x32_bf16 v[120:123], v[88:91], v[22:25], v[120:123]
	v_mfma_f32_16x16x32_bf16 v[92:95], v[84:87], v[22:25], v[92:95]
	v_mfma_f32_16x16x32_bf16 v[64:67], v[104:107], v[22:25], v[64:67]
	v_mfma_f32_16x16x32_bf16 v[48:51], v[96:99], v[22:25], v[48:51]
	v_mfma_f32_16x16x32_bf16 v[40:43], v[104:107], v[18:21], v[40:43]
	v_mfma_f32_16x16x32_bf16 v[36:39], v[96:99], v[18:21], v[36:39]
	v_mfma_f32_16x16x32_bf16 v[52:55], v[104:107], v[14:17], v[52:55]
	v_mfma_f32_16x16x32_bf16 v[44:47], v[96:99], v[14:17], v[44:47]
	s_waitcnt lgkmcnt(1)
	v_mfma_f32_16x16x32_bf16 v[96:99], v[76:79], v[22:25], v[100:103]
	v_mfma_f32_16x16x32_bf16 v[104:107], v[76:79], v[14:17], v[112:115]
	s_waitcnt lgkmcnt(0)
; #define LAS __attribute__((address_space(3)))
; template <int L>
; __device__ __forceinline__ void hyena_unit(CArgs& a, int l, int c, LAS unsigned char* lds) {
;     ...
;         for (int ib = 0; ib < 8; ++ib) {
;             const bf16* zq = zp + 256 * (ib < 7 ? ib + 1 : 7);
; #pragma unroll
;             for (int ii = 0; ii < 8; ++ii) zn[ii] = *(const bf16x8*)(zq + 32 * ii);
; #pragma unroll
;             for (int ii = 0; ii < 8; ++ii) {
;                 A[(16 - 2 * ii) & 15] = *(const LAS bf16x8*)(ap + 64 * ii);
;                 A[(17 - 2 * ii) & 15] = *(const LAS bf16x8*)(ap + 64 * ii - 32);
; #pragma unroll
;                 for (int jj = 0; jj < 16; ++jj) { const int j = (jj + 2) & 15; acc[j] = __builtin_amdgcn_mfma_f32_16x16x32_bf16(A[(j + 16 - 2 * ii) & 15], zc[ii], acc[j], 0, 0, 0); }
;             }
;             ap += 512;
; #pragma unroll
;             for (int ii = 0; ii < 8; ++ii) zc[ii] = zn[ii];
;         }
	v_mfma_f32_16x16x32_bf16 v[22:25], v[80:83], v[22:25], v[26:29]
	v_mfma_f32_16x16x32_bf16 v[26:29], v[80:83], v[18:21], v[30:33]
	v_mfma_f32_16x16x32_bf16 v[30:33], v[80:83], v[14:17], v[116:119]
	s_nop 2
	ds_read_b128 v[116:119], v161 offset:192
	ds_read_b128 v[112:115], v161 offset:160
	v_mfma_f32_16x16x32_bf16 v[100:103], v[76:79], v[18:21], v[108:111]
	v_mfma_f32_16x16x32_bf16 v[108:111], v[76:79], v[10:13], v[124:127]
	v_mfma_f32_16x16x32_bf16 v[124:127], v[80:83], v[10:13], v[128:131]
	v_mfma_f32_16x16x32_bf16 v[120:123], v[72:75], v[18:21], v[120:123]
	v_mfma_f32_16x16x32_bf16 v[92:95], v[68:71], v[18:21], v[92:95]
	v_mfma_f32_16x16x32_bf16 v[64:67], v[88:91], v[18:21], v[64:67]
	v_mfma_f32_16x16x32_bf16 v[48:51], v[84:87], v[18:21], v[48:51]
	v_mfma_f32_16x16x32_bf16 v[40:43], v[88:91], v[14:17], v[40:43]
	v_mfma_f32_16x16x32_bf16 v[36:39], v[84:87], v[14:17], v[36:39]
	v_mfma_f32_16x16x32_bf16 v[52:55], v[88:91], v[10:13], v[52:55]
	v_mfma_f32_16x16x32_bf16 v[44:47], v[84:87], v[10:13], v[44:47]
	s_waitcnt lgkmcnt(1)
	v_mfma_f32_16x16x32_bf16 v[84:87], v[116:119], v[18:21], v[96:99]
	v_mfma_f32_16x16x32_bf16 v[88:91], v[116:119], v[14:17], v[100:103]
	s_waitcnt lgkmcnt(0)
	v_mfma_f32_16x16x32_bf16 v[18:21], v[112:115], v[18:21], v[22:25]
	v_mfma_f32_16x16x32_bf16 v[22:25], v[112:115], v[14:17], v[26:29]
	v_mfma_f32_16x16x32_bf16 v[26:29], v[112:115], v[10:13], v[30:33]
	v_mfma_f32_16x16x32_bf16 v[30:33], v[116:119], v[6:9], v[108:111]
	ds_read_b128 v[100:103], v161 offset:256
	s_nop 1
	ds_read_b128 v[108:111], v161 offset:224
	v_mfma_f32_16x16x32_bf16 v[96:99], v[116:119], v[10:13], v[104:107]
	v_mfma_f32_16x16x32_bf16 v[104:107], v[112:115], v[6:9], v[124:127]
	v_mfma_f32_16x16x32_bf16 v[48:51], v[68:71], v[14:17], v[48:51]
	v_mfma_f32_16x16x32_bf16 v[36:39], v[68:71], v[10:13], v[36:39]
	v_mfma_f32_16x16x32_bf16 v[44:47], v[68:71], v[6:9], v[44:47]
	s_waitcnt lgkmcnt(1)
	v_mfma_f32_16x16x32_bf16 v[68:71], v[100:103], v[14:17], v[84:87]
	v_mfma_f32_16x16x32_bf16 v[84:87], v[100:103], v[6:9], v[96:99]
	s_waitcnt vmcnt(8) lgkmcnt(0)
	v_mfma_f32_16x16x32_bf16 v[124:127], v[108:111], v[2:5], v[104:107]
	s_nop 2
	ds_read_b128 v[104:107], v161 offset:320
	ds_read_b128 v[96:99], v161 offset:288
	v_mfma_f32_16x16x32_bf16 v[120:123], v[132:135], v[14:17], v[120:123]
	v_mfma_f32_16x16x32_bf16 v[92:95], v[136:139], v[14:17], v[92:95]
	v_mfma_f32_16x16x32_bf16 v[64:67], v[72:75], v[14:17], v[64:67]
	v_mfma_f32_16x16x32_bf16 v[14:17], v[108:111], v[14:17], v[18:21]
	v_mfma_f32_16x16x32_bf16 v[18:21], v[108:111], v[10:13], v[22:25]
	v_mfma_f32_16x16x32_bf16 v[22:25], v[108:111], v[6:9], v[26:29]
	s_waitcnt lgkmcnt(1)
	v_mfma_f32_16x16x32_bf16 v[26:29], v[104:107], v[10:13], v[68:71]
	s_nop 2
	v_mfma_f32_16x16x32_bf16 v[120:123], v[60:63], v[10:13], v[120:123]
	v_mfma_f32_16x16x32_bf16 v[92:95], v[56:59], v[10:13], v[92:95]
	v_mfma_f32_16x16x32_bf16 v[64:67], v[132:135], v[10:13], v[64:67]
	v_mfma_f32_16x16x32_bf16 v[48:51], v[136:139], v[10:13], v[48:51]
	v_mfma_f32_16x16x32_bf16 v[40:43], v[72:75], v[10:13], v[40:43]
	v_mfma_f32_16x16x32_bf16 v[52:55], v[72:75], v[6:9], v[52:55]
	v_mfma_f32_16x16x32_bf16 v[72:75], v[100:103], v[10:13], v[88:91]
	s_waitcnt lgkmcnt(0)
	v_mfma_f32_16x16x32_bf16 v[10:13], v[96:99], v[10:13], v[14:17]
	s_nop 2
	v_mfma_f32_16x16x32_bf16 v[36:39], v[136:139], v[6:9], v[36:39]
	v_mfma_f32_16x16x32_bf16 v[44:47], v[136:139], v[2:5], v[44:47]
	v_mfma_f32_16x16x32_bf16 v[136:139], v[104:107], v[2:5], v[84:87]
	ds_read_b128 v[88:91], v161 offset:384
	s_nop 1
	ds_read_b128 v[84:87], v161 offset:352
	v_mfma_f32_16x16x32_bf16 v[128:131], v[100:103], v[2:5], v[30:33]
	ds_read_b128 v[68:71], v161 offset:416
	v_mfma_f32_16x16x32_bf16 v[30:33], v[104:107], v[6:9], v[72:75]
	s_nop 2
	ds_read_b128 v[72:75], v161 offset:448
	v_mfma_f32_16x16x32_bf16 v[120:123], v[76:79], v[6:9], v[120:123]
	v_add_u32_e32 v161, 0x200, v161
	v_mfma_f32_16x16x32_bf16 v[92:95], v[80:83], v[6:9], v[92:95]
	v_mfma_f32_16x16x32_bf16 v[64:67], v[60:63], v[6:9], v[64:67]
	v_mfma_f32_16x16x32_bf16 v[48:51], v[56:59], v[6:9], v[48:51]
	v_mfma_f32_16x16x32_bf16 v[40:43], v[132:135], v[6:9], v[40:43]
	v_mfma_f32_16x16x32_bf16 v[52:55], v[132:135], v[2:5], v[52:55]
	v_mfma_f32_16x16x32_bf16 v[18:21], v[96:99], v[6:9], v[18:21]
	v_mfma_f32_16x16x32_bf16 v[132:135], v[96:99], v[2:5], v[22:25]
	s_waitcnt lgkmcnt(3)
	v_mfma_f32_16x16x32_bf16 v[22:25], v[88:91], v[6:9], v[26:29]
	s_waitcnt lgkmcnt(2)
	v_mfma_f32_16x16x32_bf16 v[6:9], v[84:87], v[6:9], v[10:13]
	s_waitcnt vmcnt(6)
	v_mov_b64_e32 v[26:27], v[170:171]
	v_mfma_f32_16x16x32_bf16 v[120:123], v[116:119], v[2:5], v[120:123]
	v_mov_b64_e32 v[28:29], v[172:173]
	s_waitcnt vmcnt(2)
	v_mov_b64_e32 v[10:11], v[186:187]
	v_mfma_f32_16x16x32_bf16 v[92:95], v[112:115], v[2:5], v[92:95]
	v_mov_b64_e32 v[12:13], v[188:189]
	v_mfma_f32_16x16x32_bf16 v[64:67], v[76:79], v[2:5], v[64:67]
	v_mfma_f32_16x16x32_bf16 v[48:51], v[80:83], v[2:5], v[48:51]
	v_mfma_f32_16x16x32_bf16 v[40:43], v[60:63], v[2:5], v[40:43]
	v_mfma_f32_16x16x32_bf16 v[36:39], v[56:59], v[2:5], v[36:39]
	v_mfma_f32_16x16x32_bf16 v[144:147], v[88:91], v[2:5], v[30:33]
	v_mfma_f32_16x16x32_bf16 v[140:143], v[84:87], v[2:5], v[18:21]
	s_nop 1
	v_mov_b64_e32 v[32:33], v[212:213]
	v_mov_b64_e32 v[30:31], v[210:211]
	v_mov_b64_e32 v[14:15], v[182:183]
	s_waitcnt lgkmcnt(0)
	v_mfma_f32_16x16x32_bf16 v[148:151], v[72:75], v[2:5], v[22:25]
	v_mov_b64_e32 v[18:19], v[178:179]
	v_mov_b64_e32 v[20:21], v[180:181]
	v_mov_b64_e32 v[16:17], v[184:185]
	v_mfma_f32_16x16x32_bf16 v[152:155], v[68:71], v[2:5], v[6:9]
	v_mov_b64_e32 v[22:23], v[174:175]
	s_waitcnt vmcnt(0)
	v_mov_b64_e32 v[2:3], v[206:207]
	v_mov_b64_e32 v[24:25], v[176:177]
	v_mov_b64_e32 v[6:7], v[202:203]
	v_mov_b64_e32 v[8:9], v[204:205]
	v_mov_b64_e32 v[4:5], v[208:209]
	s_cbranch_scc1 .LBB0_2649
; __device__ __forceinline__ unsigned pk2(float lo, float hi) { return f2bf(lo) | (f2bf(hi) << 16); }
; template <int L>
; __device__ __forceinline__ void hyena_unit(CArgs& a, int l, int c, LAS unsigned char* lds) {
;     ...
;     for (int j = 0; j < NTW; ++j) *(u32x2*)(YT + 16 * (w * NTW + j) + 4 * kg) = (u32x2){pk2(acc[j][0], acc[j][1]), pk2(acc[j][2], acc[j][3])};
;     __syncthreads();
	v_lshlrev_b32_e32 v2, 8, v1
	v_cvt_pk_bf16_f32 v6, v148, v149
	v_lshl_add_u64 v[4:5], v[156:157], 0, v[34:35]
	v_cvt_pk_bf16_f32 v7, v150, v151
	v_ashrrev_i32_e32 v3, 31, v2
	v_lshl_add_u64 v[2:3], v[2:3], 1, v[4:5]
	s_mov_b64 s[0:1], 0x50400200
	v_lshl_add_u64 v[4:5], v[2:3], 0, s[0:1]
	s_mov_b32 s0, 0x50400000
	v_add_co_u32_e32 v2, vcc, s0, v2
	s_nop 0
	s_nop 0
	v_addc_co_u32_e32 v3, vcc, 0, v3, vcc
	global_store_dwordx2 v[2:3], v[6:7], off offset:512
	v_cvt_pk_bf16_f32 v2, v152, v153
	v_cvt_pk_bf16_f32 v3, v154, v155
	global_store_dwordx2 v[4:5], v[2:3], off offset:32
	v_cvt_pk_bf16_f32 v2, v144, v145
	v_cvt_pk_bf16_f32 v3, v146, v147
	global_store_dwordx2 v[4:5], v[2:3], off offset:64
	v_cvt_pk_bf16_f32 v2, v140, v141
	v_cvt_pk_bf16_f32 v3, v142, v143
	global_store_dwordx2 v[4:5], v[2:3], off offset:96
	v_cvt_pk_bf16_f32 v2, v136, v137
	v_cvt_pk_bf16_f32 v3, v138, v139
	global_store_dwordx2 v[4:5], v[2:3], off offset:128
	v_cvt_pk_bf16_f32 v2, v132, v133
	v_cvt_pk_bf16_f32 v3, v134, v135
	global_store_dwordx2 v[4:5], v[2:3], off offset:160
	v_cvt_pk_bf16_f32 v2, v128, v129
	v_cvt_pk_bf16_f32 v3, v130, v131
	global_store_dwordx2 v[4:5], v[2:3], off offset:192
	v_cvt_pk_bf16_f32 v2, v124, v125
	v_cvt_pk_bf16_f32 v3, v126, v127
	global_store_dwordx2 v[4:5], v[2:3], off offset:224
	v_cvt_pk_bf16_f32 v2, v120, v121
	v_cvt_pk_bf16_f32 v3, v122, v123
	global_store_dwordx2 v[4:5], v[2:3], off offset:256
	v_cvt_pk_bf16_f32 v2, v92, v93
	v_cvt_pk_bf16_f32 v3, v94, v95
	global_store_dwordx2 v[4:5], v[2:3], off offset:288
	v_cvt_pk_bf16_f32 v2, v64, v65
	v_cvt_pk_bf16_f32 v3, v66, v67
	global_store_dwordx2 v[4:5], v[2:3], off offset:320
	v_cvt_pk_bf16_f32 v2, v48, v49
	v_cvt_pk_bf16_f32 v3, v50, v51
	global_store_dwordx2 v[4:5], v[2:3], off offset:352
	v_cvt_pk_bf16_f32 v2, v40, v41
	v_cvt_pk_bf16_f32 v3, v42, v43
	global_store_dwordx2 v[4:5], v[2:3], off offset:384
	v_cvt_pk_bf16_f32 v2, v36, v37
	v_cvt_pk_bf16_f32 v3, v38, v39
	global_store_dwordx2 v[4:5], v[2:3], off offset:416
	v_cvt_pk_bf16_f32 v2, v52, v53
	v_cvt_pk_bf16_f32 v3, v54, v55
	global_store_dwordx2 v[4:5], v[2:3], off offset:448
	v_cvt_pk_bf16_f32 v2, v44, v45
	v_cvt_pk_bf16_f32 v1, v46, v46
	v_lshrrev_b32_e32 v1, 16, v1
	v_cvt_pk_bf16_f32 v3, v47, v47
	v_and_or_b32 v3, v3, s80, v1
	s_mov_b64 s[14:15], -1
	global_store_dwordx2 v[4:5], v[2:3], off offset:480
	s_barrier
